# speedup vs baseline: 1.0099x; 1.0099x over previous
.LBB0_3:
	s_add_i32 s3, s2, 0xfffffe00
	s_lshr_b32 s8, s3, 3
	s_mul_i32 s9, s8, 0x2493
	s_lshr_b32 s9, s9, 16
	s_mul_i32 s10, s9, 7
	s_sub_u32 s10, s8, s10
	s_cmp_lt_u32 s10, 2
	s_cbranch_scc1 .Lcvt_work
	s_cmp_lt_u32 s9, 32
	s_cbranch_scc0 .LBB0_2
	s_lshl_b32 s9, s9, 3
	s_and_b32 s11, s3, 7
	s_or_b32 s3, s9, s11
	v_cmp_eq_u32_e32 vcc, 0, v0
	v_mov_b32_e32 v1, 0
	s_cmp_eq_u32 s10, 5
	s_cbranch_scc1 .Lcvt_mb_wo
	s_cmp_eq_u32 s10, 4
	s_cbranch_scc1 .Lcvt_mb_kv
	s_cmp_eq_u32 s10, 3
	s_cbranch_scc1 .Lcvt_mb_h2
	s_cmp_eq_u32 s10, 6
	s_cbranch_scc0 .LBB0_2
	s_cmp_eq_u32 s3, 0
	s_cbranch_scc0 .LBB0_2
	s_load_dwordx2 s[6:7], s[0:1], 0x28
	v_mov_b32_e32 v2, 0
	s_waitcnt lgkmcnt(0)
	s_add_u32 s6, s6, 0xa000000
	s_addc_u32 s7, s7, 0
	s_and_saveexec_b64 s[8:9], vcc
	s_cbranch_execz .LBB0_2
	global_store_dword v1, v2, s[6:7]
	global_store_dword v1, v2, s[6:7] offset:64
	global_store_dword v1, v2, s[6:7] offset:128
	s_endpgm

.LBB2_56:
	s_lshl_b32 s0, s2, 5
	s_lshr_b32 s1, s2, 3
	s_and_b32 s0, s0, 0x60
	s_lshl_b32 s3, s2, 1
	s_or_b32 s0, s0, s1
	v_lshrrev_b32_e32 v3, 3, v0
	v_bfe_u32 v4, v0, 2, 4
	s_and_b32 s20, s3, 8
	s_bfe_u32 s3, s2, 0x30003
	s_lshr_b32 s21, s0, 3
	v_and_or_b32 v5, v3, 48, v4
	v_or_b32_e32 v3, 64, v3
	s_movk_i32 s0, 0x70
	s_or_b32 s22, s20, s3
	v_and_or_b32 v3, v3, s0, v4
	s_lshl_b32 s0, s21, 21
	s_waitcnt lgkmcnt(0)
	s_lshl_b32 s46, s2, 16
	s_add_u32 s46, s46, 0x2000000
	s_add_u32 s44, s6, s46
	s_addc_u32 s45, s7, 0
	s_load_dwordx2 s[46:47], s[44:45], 0x0
	s_add_u32 s54, s4, 0xa000000
	s_addc_u32 s55, s5, 0
	s_mov_b32 s48, 0
	s_mov_b32 s50, 0
	s_mov_b32 s51, 0
	v_cmp_eq_u32_e64 s[56:57], 0, v0
	v_lshlrev_b32_e32 v226, 5, v0
	v_lshlrev_b32_e32 v227, 4, v0
	s_lshl_b32 s58, s2, 17
	s_add_u32 s58, s58, 0x1000
	s_add_u32 s62, s6, s58
	s_addc_u32 s63, s7, 0
	s_add_u32 s64, s4, s58
	s_addc_u32 s65, s5, 0
	s_load_dwordx4 s[68:71], s[62:63], 0x0
	v_lshrrev_b32_e32 v228, 7, v0
	v_and_b32_e32 v229, 0x7f, v0
	v_lshlrev_b32_e32 v230, 14, v228
	v_lshlrev_b32_e32 v231, 5, v229
	v_or_b32_e32 v236, v230, v231
	v_lshlrev_b32_e32 v230, 13, v228
	v_lshlrev_b32_e32 v231, 4, v229
	v_or_b32_e32 v237, v230, v231
	s_add_u32 s0, s6, s0
	v_lshlrev_b32_e32 v1, 4, v0
	v_and_b32_e32 v2, 32, v0
	s_addc_u32 s1, s7, 0
	s_add_i32 s23, 0, 0x10000
	v_bitop3_b32 v2, v1, v2, 48 bitop3:0x6c
	v_add_u32_e32 v141, s23, v1
	v_and_or_b32 v2, v0, 64, v2
	v_readfirstlane_b32 s6, v141
	v_add_u32_e32 v142, 0x2000, v141
	v_lshl_or_b32 v132, v5, 13, v2
	s_mov_b32 m0, s6
	v_readfirstlane_b32 s6, v142
	global_load_lds_dwordx4 v132, s[0:1]
	s_mov_b32 m0, s6
	s_lshl_b32 s6, s22, 21
	s_add_u32 s6, s4, s6
	s_addc_u32 s7, s5, 0
	v_add_u32_e32 v140, 0, v1
	s_add_u32 s16, s0, 0x100000
	v_lshl_or_b32 v130, v3, 13, v2
	v_readfirstlane_b32 s14, v140
	v_add_u32_e32 v144, 0x2000, v140
	s_addc_u32 s17, s1, 0
	s_add_i32 s24, 0, 0x14000
	global_load_lds_dwordx4 v130, s[0:1]
	s_mov_b32 m0, s14
	v_readfirstlane_b32 s14, v144
	v_add_u32_e32 v145, s24, v1
	global_load_lds_dwordx4 v132, s[6:7]
	s_mov_b32 m0, s14
	v_readfirstlane_b32 s14, v145
	v_add_u32_e32 v146, 0x2000, v145
	global_load_lds_dwordx4 v130, s[6:7]
	s_mov_b32 m0, s14
	v_readfirstlane_b32 s14, v146
	v_add_u32_e32 v148, 0x4000, v140
	global_load_lds_dwordx4 v132, s[16:17]
	s_mov_b32 m0, s14
	s_add_u32 s14, s6, 0x100000
	v_readfirstlane_b32 s18, v148
	v_add_u32_e32 v149, 0x6000, v140
	global_load_lds_dwordx4 v130, s[16:17]
	s_addc_u32 s15, s7, 0
	s_mov_b32 m0, s18
	v_readfirstlane_b32 s18, v149
	global_load_lds_dwordx4 v132, s[14:15]
	s_mov_b32 m0, s18
	v_lshrrev_b32_e32 v2, 8, v0
	global_load_lds_dwordx4 v130, s[14:15]
	v_mov_b32_e32 v133, 0
	v_mov_b32_e32 v131, v133
	v_cmp_eq_u32_e32 vcc, 1, v2
	s_and_saveexec_b64 s[18:19], vcc
	s_cbranch_execz .LBB2_58
	s_barrier

.LBB2_59:
	ds_read_b128 v[160:163], v157
	ds_read_b128 v[164:167], v157 offset:1024
	ds_read_b128 v[168:171], v157 offset:2048
	ds_read_b128 v[172:175], v157 offset:3072
	s_add_u32 s24, s4, s2
	s_addc_u32 s25, s5, s3
	s_add_u32 s24, s24, 0x80
	s_addc_u32 s25, s25, 0
	v_readfirstlane_b32 s26, v158
	v_lshl_add_u64 v[176:177], s[24:25], 0, v[132:133]
	s_mov_b32 m0, s26
	s_nop 0
	global_load_lds_dwordx4 v[176:177], off
	v_lshl_add_u64 v[176:177], s[24:25], 0, v[130:131]
	v_readfirstlane_b32 s24, v159
	s_mov_b32 m0, s24
	s_nop 0
	global_load_lds_dwordx4 v[176:177], off
	ds_read_b128 v[176:179], v138
	ds_read_b128 v[180:183], v138 offset:1024
	ds_read_b128 v[184:187], v137
	ds_read_b128 v[188:191], v137 offset:1024
	ds_read_b128 v[192:195], v136
	ds_read_b128 v[196:199], v136 offset:1024
	ds_read_b128 v[200:203], v135
	ds_read_b128 v[204:207], v135 offset:1024
	s_waitcnt lgkmcnt(8)
	s_barrier
	s_waitcnt lgkmcnt(0)
	s_setprio 1
	s_waitcnt lgkmcnt(0)
	v_mfma_f32_16x16x32_f16 v[126:129], v[160:163], v[176:179], v[126:129]
	v_mfma_f32_16x16x32_f16 v[122:125], v[168:171], v[176:179], v[122:125]
	v_mfma_f32_16x16x32_f16 v[118:121], v[160:163], v[184:187], v[118:121]
	v_mfma_f32_16x16x32_f16 v[114:117], v[168:171], v[184:187], v[114:117]
	v_mfma_f32_16x16x32_f16 v[110:113], v[160:163], v[192:195], v[110:113]
	v_mfma_f32_16x16x32_f16 v[106:109], v[168:171], v[192:195], v[106:109]
	v_mfma_f32_16x16x32_f16 v[102:105], v[160:163], v[200:203], v[102:105]
	v_mfma_f32_16x16x32_f16 v[98:101], v[168:171], v[200:203], v[98:101]
	v_mfma_f32_16x16x32_f16 v[126:129], v[164:167], v[180:183], v[126:129]
	v_mfma_f32_16x16x32_f16 v[122:125], v[172:175], v[180:183], v[122:125]
	v_mfma_f32_16x16x32_f16 v[118:121], v[164:167], v[188:191], v[118:121]
	v_mfma_f32_16x16x32_f16 v[114:117], v[172:175], v[188:191], v[114:117]
	v_mfma_f32_16x16x32_f16 v[110:113], v[164:167], v[196:199], v[110:113]
	v_mfma_f32_16x16x32_f16 v[106:109], v[172:175], v[196:199], v[106:109]
	v_mfma_f32_16x16x32_f16 v[102:105], v[164:167], v[204:207], v[102:105]
	v_mfma_f32_16x16x32_f16 v[98:101], v[172:175], v[204:207], v[98:101]
	s_setprio 0
	s_barrier
	s_add_u32 s26, s0, s2
	s_addc_u32 s27, s1, s3
	s_add_u32 s24, s26, 0x100
	s_addc_u32 s25, s27, 0
	v_readfirstlane_b32 s28, v141
	v_lshl_add_u64 v[224:225], s[24:25], 0, v[132:133]
	s_mov_b32 m0, s28
	ds_read_b128 v[208:211], v153
	ds_read_b128 v[212:215], v153 offset:1024
	ds_read_b128 v[216:219], v153 offset:2048
	ds_read_b128 v[220:223], v153 offset:3072
	global_load_lds_dwordx4 v[224:225], off
	v_lshl_add_u64 v[224:225], s[24:25], 0, v[130:131]
	v_readfirstlane_b32 s24, v142
	s_mov_b32 m0, s24
	s_nop 0
	global_load_lds_dwordx4 v[224:225], off
	s_barrier
	s_waitcnt lgkmcnt(0)
	s_setprio 1
	s_waitcnt lgkmcnt(0)
	v_mfma_f32_16x16x32_f16 v[94:97], v[208:211], v[176:179], v[94:97]
	v_mfma_f32_16x16x32_f16 v[90:93], v[216:219], v[176:179], v[90:93]
	v_mfma_f32_16x16x32_f16 v[86:89], v[208:211], v[184:187], v[86:89]
	v_mfma_f32_16x16x32_f16 v[82:85], v[216:219], v[184:187], v[82:85]
	v_mfma_f32_16x16x32_f16 v[78:81], v[208:211], v[192:195], v[78:81]
	v_mfma_f32_16x16x32_f16 v[74:77], v[216:219], v[192:195], v[74:77]
	v_mfma_f32_16x16x32_f16 v[70:73], v[208:211], v[200:203], v[70:73]
	v_mfma_f32_16x16x32_f16 v[66:69], v[216:219], v[200:203], v[66:69]
	v_mfma_f32_16x16x32_f16 v[94:97], v[212:215], v[180:183], v[94:97]
	v_mfma_f32_16x16x32_f16 v[90:93], v[220:223], v[180:183], v[90:93]
	v_mfma_f32_16x16x32_f16 v[86:89], v[212:215], v[188:191], v[86:89]
	v_mfma_f32_16x16x32_f16 v[82:85], v[220:223], v[188:191], v[82:85]
	v_mfma_f32_16x16x32_f16 v[78:81], v[212:215], v[196:199], v[78:81]
	v_mfma_f32_16x16x32_f16 v[74:77], v[220:223], v[196:199], v[74:77]
	v_mfma_f32_16x16x32_f16 v[70:73], v[212:215], v[204:207], v[70:73]
	v_mfma_f32_16x16x32_f16 v[66:69], v[220:223], v[204:207], v[66:69]
	s_setprio 0
	s_add_u32 s28, s6, s2
	s_addc_u32 s29, s7, s3
	s_add_u32 s24, s28, 0x100
	s_addc_u32 s25, s29, 0
	v_readfirstlane_b32 s30, v140
	v_lshl_add_u64 v[224:225], s[24:25], 0, v[132:133]
	s_mov_b32 m0, s30
	s_barrier
	ds_read_b128 v[176:179], v138 offset:16384
	ds_read_b128 v[180:183], v138 offset:17408
	ds_read_b128 v[184:187], v137 offset:16384
	ds_read_b128 v[188:191], v137 offset:17408
	ds_read_b128 v[192:195], v136 offset:16384
	ds_read_b128 v[196:199], v136 offset:17408
	ds_read_b128 v[200:203], v135 offset:16384
	ds_read_b128 v[204:207], v135 offset:17408
	global_load_lds_dwordx4 v[224:225], off
	v_lshl_add_u64 v[224:225], s[24:25], 0, v[130:131]
	v_readfirstlane_b32 s24, v144
	s_mov_b32 m0, s24
	s_nop 0
	global_load_lds_dwordx4 v[224:225], off
	s_barrier
	s_waitcnt lgkmcnt(0)
	s_setprio 1
	s_waitcnt lgkmcnt(0)
	v_mfma_f32_16x16x32_f16 v[62:65], v[160:163], v[176:179], v[62:65]
	v_mfma_f32_16x16x32_f16 v[58:61], v[168:171], v[176:179], v[58:61]
	v_mfma_f32_16x16x32_f16 v[54:57], v[160:163], v[184:187], v[54:57]
	v_mfma_f32_16x16x32_f16 v[50:53], v[168:171], v[184:187], v[50:53]
	v_mfma_f32_16x16x32_f16 v[46:49], v[160:163], v[192:195], v[46:49]
	v_mfma_f32_16x16x32_f16 v[42:45], v[168:171], v[192:195], v[42:45]
	v_mfma_f32_16x16x32_f16 v[38:41], v[160:163], v[200:203], v[38:41]
	v_mfma_f32_16x16x32_f16 v[34:37], v[168:171], v[200:203], v[34:37]
	v_mfma_f32_16x16x32_f16 v[62:65], v[164:167], v[180:183], v[62:65]
	v_mfma_f32_16x16x32_f16 v[58:61], v[172:175], v[180:183], v[58:61]
	v_mfma_f32_16x16x32_f16 v[54:57], v[164:167], v[188:191], v[54:57]
	v_mfma_f32_16x16x32_f16 v[50:53], v[172:175], v[188:191], v[50:53]
	v_mfma_f32_16x16x32_f16 v[46:49], v[164:167], v[196:199], v[46:49]
	v_mfma_f32_16x16x32_f16 v[42:45], v[172:175], v[196:199], v[42:45]
	v_mfma_f32_16x16x32_f16 v[38:41], v[164:167], v[204:207], v[38:41]
	v_mfma_f32_16x16x32_f16 v[34:37], v[172:175], v[204:207], v[34:37]
	s_setprio 0
	s_barrier
	s_add_u32 s30, s16, s2
	s_addc_u32 s31, s17, s3
	s_add_u32 s24, s30, 0x100
	s_addc_u32 s25, s31, 0
	v_readfirstlane_b32 s33, v145
	v_lshl_add_u64 v[160:161], s[24:25], 0, v[132:133]
	s_mov_b32 m0, s33
	s_nop 0
	global_load_lds_dwordx4 v[160:161], off
	v_lshl_add_u64 v[160:161], s[24:25], 0, v[130:131]
	v_readfirstlane_b32 s24, v146
	s_mov_b32 m0, s24
	s_nop 0
	global_load_lds_dwordx4 v[160:161], off
	s_mov_b32 s49, s48
	s_add_i32 s48, s48, 1
	s_cmp_gt_u32 s49, 26
	s_cbranch_scc1 .Ls1_plain
	s_cmp_eq_u32 s49, 0
	s_cbranch_scc1 .Ls1_a0
	s_cmp_lt_u32 s49, 8
	s_cbranch_scc1 .Ls1_am
	s_cmp_eq_u32 s49, 8
	s_cbranch_scc1 .Ls1_al
	s_cmp_eq_u32 s49, 9
	s_cbranch_scc1 .Ls1_b0
	s_cmp_lt_u32 s49, 17
	s_cbranch_scc1 .Ls1_bm
	s_cmp_eq_u32 s49, 17
	s_cbranch_scc1 .Ls1_bl
	s_cmp_eq_u32 s49, 18
	s_cbranch_scc1 .Ls1_k0
	s_cmp_lt_u32 s49, 26
	s_cbranch_scc1 .Ls1_km
	s_cmp_eq_u32 s49, 26
	s_cbranch_scc1 .Ls1_kl

.Ls1_a0:
	s_mov_b32 s59, 0
	s_cmp_lt_u32 s59, 4
	s_cselect_b32 s52, s68, s70
	s_cselect_b32 s53, s69, s71
	s_and_b32 s58, s59, 3
	s_lshl_b32 s58, s58, 16
	s_add_u32 s52, s52, s58
	s_addc_u32 s53, s53, 0
	global_load_dwordx4 v[228:231], v236, s[52:53] nt
	global_load_dwordx4 v[232:235], v236, s[52:53] offset:16 nt
	s_waitcnt vmcnt(8)
	s_branch .Ls1_join
.Ls1_am:
	s_sub_u32 s59, s49, 1
	s_waitcnt vmcnt(16)
	v_cvt_pk_f16_f32 v228, v228, v229
	v_cvt_pk_f16_f32 v229, v230, v231
	v_cvt_pk_f16_f32 v230, v232, v233
	v_cvt_pk_f16_f32 v231, v234, v235
	s_cmp_lt_u32 s59, 4
	s_cselect_b32 s52, s62, s64
	s_cselect_b32 s53, s63, s65
	s_and_b32 s58, s59, 3
	s_lshl_b32 s58, s58, 15
	s_add_u32 s52, s52, s58
	s_addc_u32 s53, s53, 0
	global_store_dwordx4 v237, v[228:231], s[52:53] sc1
	s_add_u32 s59, s59, 1
	s_cmp_lt_u32 s59, 4
	s_cselect_b32 s52, s68, s70
	s_cselect_b32 s53, s69, s71
	s_and_b32 s58, s59, 3
	s_lshl_b32 s58, s58, 16
	s_add_u32 s52, s52, s58
	s_addc_u32 s53, s53, 0
	global_load_dwordx4 v[228:231], v236, s[52:53] nt
	global_load_dwordx4 v[232:235], v236, s[52:53] offset:16 nt
	s_waitcnt vmcnt(9)
	s_branch .Ls1_join
.Ls1_al:
	s_mov_b32 s59, 7
	s_waitcnt vmcnt(16)
	v_cvt_pk_f16_f32 v228, v228, v229
	v_cvt_pk_f16_f32 v229, v230, v231
	v_cvt_pk_f16_f32 v230, v232, v233
	v_cvt_pk_f16_f32 v231, v234, v235
	s_cmp_lt_u32 s59, 4
	s_cselect_b32 s52, s62, s64
	s_cselect_b32 s53, s63, s65
	s_and_b32 s58, s59, 3
	s_lshl_b32 s58, s58, 15
	s_add_u32 s52, s52, s58
	s_addc_u32 s53, s53, 0
	global_store_dwordx4 v237, v[228:231], s[52:53] sc1
	s_waitcnt vmcnt(7)
	s_branch .Ls1_join
.Ls1_b0:
	s_mov_b32 s59, 0
	s_cmp_lt_u32 s59, 4
	s_cselect_b32 s52, s68, s70
	s_cselect_b32 s53, s69, s71
	s_and_b32 s58, s59, 3
	s_lshl_b32 s58, s58, 16
	s_add_u32 s58, s58, 0x1000
	s_add_u32 s52, s52, s58
	s_addc_u32 s53, s53, 0
	global_load_dwordx4 v[228:231], v236, s[52:53] nt
	global_load_dwordx4 v[232:235], v236, s[52:53] offset:16 nt
	s_waitcnt vmcnt(8)
	s_branch .Ls1_join
.Ls1_bm:
	s_sub_u32 s59, s49, 10
	s_waitcnt vmcnt(16)
	v_cvt_pk_f16_f32 v228, v228, v229
	v_cvt_pk_f16_f32 v229, v230, v231
	v_cvt_pk_f16_f32 v230, v232, v233
	v_cvt_pk_f16_f32 v231, v234, v235
	s_cmp_lt_u32 s59, 4
	s_cselect_b32 s52, s62, s64
	s_cselect_b32 s53, s63, s65
	s_and_b32 s58, s59, 3
	s_lshl_b32 s58, s58, 15
	s_add_u32 s58, s58, 0x800
	s_add_u32 s52, s52, s58
	s_addc_u32 s53, s53, 0
	global_store_dwordx4 v237, v[228:231], s[52:53] sc1
	s_add_u32 s59, s59, 1
	s_cmp_lt_u32 s59, 4
	s_cselect_b32 s52, s68, s70
	s_cselect_b32 s53, s69, s71
	s_and_b32 s58, s59, 3
	s_lshl_b32 s58, s58, 16
	s_add_u32 s58, s58, 0x1000
	s_add_u32 s52, s52, s58
	s_addc_u32 s53, s53, 0
	global_load_dwordx4 v[228:231], v236, s[52:53] nt
	global_load_dwordx4 v[232:235], v236, s[52:53] offset:16 nt
	s_waitcnt vmcnt(9)
	s_branch .Ls1_join
.Ls1_bl:
	s_mov_b32 s59, 7
	s_waitcnt vmcnt(16)
	v_cvt_pk_f16_f32 v228, v228, v229
	v_cvt_pk_f16_f32 v229, v230, v231
	v_cvt_pk_f16_f32 v230, v232, v233
	v_cvt_pk_f16_f32 v231, v234, v235
	s_cmp_lt_u32 s59, 4
	s_cselect_b32 s52, s62, s64
	s_cselect_b32 s53, s63, s65
	s_and_b32 s58, s59, 3
	s_lshl_b32 s58, s58, 15
	s_add_u32 s58, s58, 0x800
	s_add_u32 s52, s52, s58
	s_addc_u32 s53, s53, 0
	global_store_dwordx4 v237, v[228:231], s[52:53] sc1
	s_waitcnt vmcnt(7)
	s_branch .Ls1_join

.Ls1_km:
	s_sub_u32 s59, s49, 19
	s_waitcnt vmcnt(16)
	v_cvt_pk_f16_f32 v228, v228, v229
	v_cvt_pk_f16_f32 v229, v230, v231
	v_cvt_pk_f16_f32 v230, v232, v233
	v_cvt_pk_f16_f32 v231, v234, v235
	s_lshl_b32 s58, s59, 13
	s_add_u32 s52, s44, s58
	s_addc_u32 s53, s45, 0
	global_store_dwordx4 v227, v[228:231], s[52:53] sc1
	s_add_u32 s59, s59, 1
	s_lshl_b32 s58, s59, 14
	s_add_u32 s52, s46, s58
	s_addc_u32 s53, s47, 0
	global_load_dwordx4 v[228:231], v226, s[52:53] nt
	global_load_dwordx4 v[232:235], v226, s[52:53] offset:16 nt
	s_waitcnt vmcnt(9)
	s_branch .Ls1_join
.Ls1_kl:
	s_mov_b32 s59, 7
	s_waitcnt vmcnt(16)
	v_cvt_pk_f16_f32 v228, v228, v229
	v_cvt_pk_f16_f32 v229, v230, v231
	v_cvt_pk_f16_f32 v230, v232, v233
	v_cvt_pk_f16_f32 v231, v234, v235
	s_lshl_b32 s58, s59, 13
	s_add_u32 s52, s44, s58
	s_addc_u32 s53, s45, 0
	global_store_dwordx4 v227, v[228:231], s[52:53] sc1
	s_waitcnt vmcnt(7)
	s_branch .Ls1_join
.Ls1_join:
	s_barrier
	s_setprio 1
	v_mfma_f32_16x16x32_f16 v[30:33], v[208:211], v[176:179], v[30:33]
	v_mfma_f32_16x16x32_f16 v[26:29], v[216:219], v[176:179], v[26:29]
	v_mfma_f32_16x16x32_f16 v[22:25], v[208:211], v[184:187], v[22:25]
	v_mfma_f32_16x16x32_f16 v[18:21], v[216:219], v[184:187], v[18:21]
	v_mfma_f32_16x16x32_f16 v[14:17], v[208:211], v[192:195], v[14:17]
	v_mfma_f32_16x16x32_f16 v[10:13], v[216:219], v[192:195], v[10:13]
	v_mfma_f32_16x16x32_f16 v[6:9], v[208:211], v[200:203], v[6:9]
	v_mfma_f32_16x16x32_f16 v[2:5], v[216:219], v[200:203], v[2:5]
	v_mfma_f32_16x16x32_f16 v[30:33], v[212:215], v[180:183], v[30:33]
	v_mfma_f32_16x16x32_f16 v[26:29], v[220:223], v[180:183], v[26:29]
	v_mfma_f32_16x16x32_f16 v[22:25], v[212:215], v[188:191], v[22:25]
	v_mfma_f32_16x16x32_f16 v[18:21], v[220:223], v[188:191], v[18:21]
	v_mfma_f32_16x16x32_f16 v[14:17], v[212:215], v[196:199], v[14:17]
	v_mfma_f32_16x16x32_f16 v[10:13], v[220:223], v[196:199], v[10:13]
	v_mfma_f32_16x16x32_f16 v[6:9], v[212:215], v[204:207], v[6:9]
	v_mfma_f32_16x16x32_f16 v[2:5], v[220:223], v[204:207], v[2:5]
	s_setprio 0
	s_barrier
	ds_read_b128 v[160:163], v143
	ds_read_b128 v[164:167], v143 offset:1024
	ds_read_b128 v[168:171], v143 offset:2048
	ds_read_b128 v[172:175], v143 offset:3072
	s_add_u32 s24, s18, s2
	s_addc_u32 s25, s19, s3
	v_readfirstlane_b32 s33, v148
	v_lshl_add_u64 v[208:209], s[24:25], 0, v[132:133]
	s_mov_b32 m0, s33
	ds_read_b128 v[176:179], v138 offset:32768
	ds_read_b128 v[180:183], v138 offset:33792
	ds_read_b128 v[184:187], v137 offset:32768
	ds_read_b128 v[188:191], v137 offset:33792
	ds_read_b128 v[192:195], v136 offset:32768
	ds_read_b128 v[196:199], v136 offset:33792
	ds_read_b128 v[200:203], v135 offset:32768
	ds_read_b128 v[204:207], v135 offset:33792
	global_load_lds_dwordx4 v[208:209], off
	v_lshl_add_u64 v[208:209], s[24:25], 0, v[130:131]
	v_readfirstlane_b32 s24, v149
	s_mov_b32 m0, s24
	s_nop 0
	global_load_lds_dwordx4 v[208:209], off
	s_waitcnt lgkmcnt(8)
	s_barrier
	s_waitcnt lgkmcnt(0)
	s_setprio 1
	s_waitcnt lgkmcnt(0)
	v_mfma_f32_16x16x32_f16 v[126:129], v[160:163], v[176:179], v[126:129]
	v_mfma_f32_16x16x32_f16 v[122:125], v[168:171], v[176:179], v[122:125]
	v_mfma_f32_16x16x32_f16 v[118:121], v[160:163], v[184:187], v[118:121]
	v_mfma_f32_16x16x32_f16 v[114:117], v[168:171], v[184:187], v[114:117]
	v_mfma_f32_16x16x32_f16 v[110:113], v[160:163], v[192:195], v[110:113]
	v_mfma_f32_16x16x32_f16 v[106:109], v[168:171], v[192:195], v[106:109]
	v_mfma_f32_16x16x32_f16 v[102:105], v[160:163], v[200:203], v[102:105]
	v_mfma_f32_16x16x32_f16 v[98:101], v[168:171], v[200:203], v[98:101]
	v_mfma_f32_16x16x32_f16 v[126:129], v[164:167], v[180:183], v[126:129]
	v_mfma_f32_16x16x32_f16 v[122:125], v[172:175], v[180:183], v[122:125]
	v_mfma_f32_16x16x32_f16 v[118:121], v[164:167], v[188:191], v[118:121]
	v_mfma_f32_16x16x32_f16 v[114:117], v[172:175], v[188:191], v[114:117]
	v_mfma_f32_16x16x32_f16 v[110:113], v[164:167], v[196:199], v[110:113]
	v_mfma_f32_16x16x32_f16 v[106:109], v[172:175], v[196:199], v[106:109]
	v_mfma_f32_16x16x32_f16 v[102:105], v[164:167], v[204:207], v[102:105]
	v_mfma_f32_16x16x32_f16 v[98:101], v[172:175], v[204:207], v[98:101]
	s_setprio 0
	s_barrier
	s_add_u32 s24, s26, 0x180
	s_addc_u32 s25, s27, 0
	v_readfirstlane_b32 s26, v150
	v_lshl_add_u64 v[224:225], s[24:25], 0, v[132:133]
	s_mov_b32 m0, s26
	ds_read_b128 v[208:211], v139
	ds_read_b128 v[212:215], v139 offset:1024
	ds_read_b128 v[216:219], v139 offset:2048
	ds_read_b128 v[220:223], v139 offset:3072
	global_load_lds_dwordx4 v[224:225], off
	v_lshl_add_u64 v[224:225], s[24:25], 0, v[130:131]
	v_readfirstlane_b32 s24, v151
	s_mov_b32 m0, s24
	s_nop 0
	global_load_lds_dwordx4 v[224:225], off
	s_barrier
	s_waitcnt lgkmcnt(0)
	s_setprio 1
	s_waitcnt lgkmcnt(0)
	v_mfma_f32_16x16x32_f16 v[94:97], v[208:211], v[176:179], v[94:97]
	v_mfma_f32_16x16x32_f16 v[90:93], v[216:219], v[176:179], v[90:93]
	v_mfma_f32_16x16x32_f16 v[86:89], v[208:211], v[184:187], v[86:89]
	v_mfma_f32_16x16x32_f16 v[82:85], v[216:219], v[184:187], v[82:85]
	v_mfma_f32_16x16x32_f16 v[78:81], v[208:211], v[192:195], v[78:81]
	v_mfma_f32_16x16x32_f16 v[74:77], v[216:219], v[192:195], v[74:77]
	v_mfma_f32_16x16x32_f16 v[70:73], v[208:211], v[200:203], v[70:73]
	v_mfma_f32_16x16x32_f16 v[66:69], v[216:219], v[200:203], v[66:69]
	v_mfma_f32_16x16x32_f16 v[94:97], v[212:215], v[180:183], v[94:97]
	v_mfma_f32_16x16x32_f16 v[90:93], v[220:223], v[180:183], v[90:93]
	v_mfma_f32_16x16x32_f16 v[86:89], v[212:215], v[188:191], v[86:89]
	v_mfma_f32_16x16x32_f16 v[82:85], v[220:223], v[188:191], v[82:85]
	v_mfma_f32_16x16x32_f16 v[78:81], v[212:215], v[196:199], v[78:81]
	v_mfma_f32_16x16x32_f16 v[74:77], v[220:223], v[196:199], v[74:77]
	v_mfma_f32_16x16x32_f16 v[70:73], v[212:215], v[204:207], v[70:73]
	v_mfma_f32_16x16x32_f16 v[66:69], v[220:223], v[204:207], v[66:69]
	s_setprio 0
	s_add_u32 s24, s28, 0x180
	s_addc_u32 s25, s29, 0
	v_readfirstlane_b32 s26, v152
	v_lshl_add_u64 v[224:225], s[24:25], 0, v[132:133]
	s_mov_b32 m0, s26
	s_barrier
	ds_read_b128 v[176:179], v138 offset:49152
	ds_read_b128 v[180:183], v138 offset:50176
	ds_read_b128 v[184:187], v137 offset:49152
	ds_read_b128 v[188:191], v137 offset:50176
	ds_read_b128 v[192:195], v136 offset:49152
	ds_read_b128 v[196:199], v136 offset:50176
	ds_read_b128 v[200:203], v135 offset:49152
	ds_read_b128 v[204:207], v135 offset:50176
	global_load_lds_dwordx4 v[224:225], off
	v_lshl_add_u64 v[224:225], s[24:25], 0, v[130:131]
	v_readfirstlane_b32 s24, v154
	s_mov_b32 m0, s24
	s_nop 0
	global_load_lds_dwordx4 v[224:225], off
	s_barrier
	s_waitcnt lgkmcnt(0)
	s_setprio 1
	s_waitcnt lgkmcnt(0)
	v_mfma_f32_16x16x32_f16 v[62:65], v[160:163], v[176:179], v[62:65]
	v_mfma_f32_16x16x32_f16 v[58:61], v[168:171], v[176:179], v[58:61]
	v_mfma_f32_16x16x32_f16 v[54:57], v[160:163], v[184:187], v[54:57]
	v_mfma_f32_16x16x32_f16 v[50:53], v[168:171], v[184:187], v[50:53]
	v_mfma_f32_16x16x32_f16 v[46:49], v[160:163], v[192:195], v[46:49]
	v_mfma_f32_16x16x32_f16 v[42:45], v[168:171], v[192:195], v[42:45]
	v_mfma_f32_16x16x32_f16 v[38:41], v[160:163], v[200:203], v[38:41]
	v_mfma_f32_16x16x32_f16 v[34:37], v[168:171], v[200:203], v[34:37]
	v_mfma_f32_16x16x32_f16 v[62:65], v[164:167], v[180:183], v[62:65]
	v_mfma_f32_16x16x32_f16 v[58:61], v[172:175], v[180:183], v[58:61]
	v_mfma_f32_16x16x32_f16 v[54:57], v[164:167], v[188:191], v[54:57]
	v_mfma_f32_16x16x32_f16 v[50:53], v[172:175], v[188:191], v[50:53]
	v_mfma_f32_16x16x32_f16 v[46:49], v[164:167], v[196:199], v[46:49]
	v_mfma_f32_16x16x32_f16 v[42:45], v[172:175], v[196:199], v[42:45]
	v_mfma_f32_16x16x32_f16 v[38:41], v[164:167], v[204:207], v[38:41]
	v_mfma_f32_16x16x32_f16 v[34:37], v[172:175], v[204:207], v[34:37]
	s_setprio 0
	s_barrier
	s_add_u32 s24, s30, 0x180
	s_addc_u32 s25, s31, 0
	v_readfirstlane_b32 s26, v155
	v_lshl_add_u64 v[160:161], s[24:25], 0, v[132:133]
	s_mov_b32 m0, s26
	s_nop 0
	global_load_lds_dwordx4 v[160:161], off
	v_lshl_add_u64 v[160:161], s[24:25], 0, v[130:131]
	v_readfirstlane_b32 s24, v156
	s_mov_b32 m0, s24
	s_nop 0
	global_load_lds_dwordx4 v[160:161], off
	s_cmp_eq_u32 s49, 9
	s_cbranch_scc1 .Ls2_arr2
	s_cmp_eq_u32 s49, 12
	s_cbranch_scc1 .Ls2_poll2
	s_cmp_eq_u32 s49, 18
	s_cbranch_scc1 .Ls2_arr3
	s_cmp_eq_u32 s49, 21
	s_cbranch_scc1 .Ls2_poll3

.Ls2_arr2:
	s_and_saveexec_b64 s[52:53], s[56:57]
	s_cbranch_execz .Ls2_arr2_no
	v_mov_b32_e32 v238, 0
	v_mov_b32_e32 v239, 1
	global_atomic_add v238, v239, s[54:55] offset:64 sc1
	s_or_b64 exec, exec, s[52:53]
	s_waitcnt vmcnt(7)
	s_branch .Ls2_join

.Ls2_arr3:
	s_and_saveexec_b64 s[52:53], s[56:57]
	s_cbranch_execz .Ls2_arr3_no
	v_mov_b32_e32 v238, 0
	v_mov_b32_e32 v239, 1
	global_atomic_add v238, v239, s[54:55] offset:128 sc1
	s_or_b64 exec, exec, s[52:53]
	s_waitcnt vmcnt(7)
	s_branch .Ls2_join

.Ls2_poll2:
	s_cmp_eq_u64 s[56:57], 0
	s_cbranch_scc1 .Ls2_plain
	s_mov_b32 s58, 0
	v_mov_b32_e32 v238, 0
.Ls2_spin2:
	global_load_dword v239, v238, s[54:55] offset:64 sc1
	s_waitcnt vmcnt(0)
	v_readfirstlane_b32 s59, v239
	s_cmp_ge_u32 s59, 0x100
	s_cbranch_scc1 .Ls2_plain
	s_add_i32 s58, s58, 1
	s_cmp_lt_u32 s58, 0x190
	s_cbranch_scc0 .Ls2_plain
	s_sleep 4
	s_branch .Ls2_spin2

.Ls2_spin3:
	global_load_dword v239, v238, s[54:55] offset:128 sc1
	s_waitcnt vmcnt(0)
	v_readfirstlane_b32 s59, v239
	s_cmp_ge_u32 s59, 0x100
	s_cbranch_scc1 .Ls2_plain
	s_add_i32 s58, s58, 1
	s_cmp_lt_u32 s58, 0x190
	s_cbranch_scc0 .Ls2_plain
	s_sleep 4
	s_branch .Ls2_spin3
